# GEMM K-loops: last 2 of each 6-piece LDS-DMA batch issued inside the following MFMA block, mid-block setprio flip pairs removed; stacked on hoisted constants + unscaled fp8 MFMA + NSA mask
# baseline (speedup 1.0000x reference)
.Lp1_join:
	ds_read_b128 v[136:139], v129
	ds_read_b128 v[144:147], v129 offset:2048
	ds_read_b128 v[140:143], v130
	ds_read_b128 v[148:151], v130 offset:2048
	v_add_u32_e32 v129, s86, v246
	v_add_u32_e32 v130, s86, v247
	ds_read_b128 v[152:155], v129
	ds_read_b128 v[160:163], v129 offset:2048
	ds_read_b128 v[156:159], v130
	ds_read_b128 v[164:167], v130 offset:2048
	s_add_i32 s10, s97, 0xffffff80
	s_add_i32 s11, s10, s94
	s_cmpk_eq_i32 s97, 0x880
	s_cselect_b32 s40, s37, s91
	s_cselect_b32 s10, 0, s10
	s_cselect_b32 s39, 0x80, s97
	s_cselect_b32 s38, s36, s11
	s_add_i32 s11, s91, s97
	s_add_i32 s39, s40, s39
	s_addk_i32 s11, 0xff00
	s_add_i32 s40, s40, s10
	s_mov_b32 m0, s72
	ds_read_b128 v[168:171], v252
	ds_read_b128 v[176:179], v252 offset:2048
	ds_read_b128 v[172:175], v253
	ds_read_b128 v[180:183], v253 offset:2048
	ds_read_b128 v[184:187], v252 offset:4096
	ds_read_b128 v[192:195], v252 offset:6144
	ds_read_b128 v[188:191], v253 offset:4096
	ds_read_b128 v[196:199], v253 offset:6144
	buffer_load_dwordx4 v250, s[12:15], s11 offen lds
	s_mov_b32 m0, s75
	s_nop 0
	buffer_load_dwordx4 v251, s[12:15], s11 offen lds
	s_waitcnt vmcnt(8)
	s_waitcnt lgkmcnt(0)
	s_barrier
	s_setprio 1
	s_waitcnt lgkmcnt(5)
	v_mfma_f32_16x16x128_f8f6f4 v[124:127], v[136:143], v[168:175], v[124:127]
	v_mfma_f32_16x16x128_f8f6f4 v[120:123], v[144:151], v[168:175], v[120:123]
	s_waitcnt lgkmcnt(4)
	v_mfma_f32_16x16x128_f8f6f4 v[112:115], v[136:143], v[176:183], v[112:115]
	v_mfma_f32_16x16x128_f8f6f4 v[104:107], v[144:151], v[176:183], v[104:107]
	s_waitcnt lgkmcnt(1)
	v_mfma_f32_16x16x128_f8f6f4 v[96:99], v[136:143], v[184:191], v[96:99]
	v_mfma_f32_16x16x128_f8f6f4 v[128:131], v[144:151], v[184:191], v[88:91]
	s_waitcnt lgkmcnt(0)
	v_mfma_f32_16x16x128_f8f6f4 v[200:203], v[136:143], v[192:199], v[80:83]
	v_mfma_f32_16x16x128_f8f6f4 v[204:207], v[144:151], v[192:199], v[72:75]
	v_mfma_f32_16x16x128_f8f6f4 v[116:119], v[152:159], v[168:175], v[116:119]
	v_mfma_f32_16x16x128_f8f6f4 v[108:111], v[160:167], v[168:175], v[108:111]
	v_mfma_f32_16x16x128_f8f6f4 v[100:103], v[152:159], v[176:183], v[100:103]
	v_mfma_f32_16x16x128_f8f6f4 v[168:171], v[160:167], v[176:183], v[92:95]
	v_mfma_f32_16x16x128_f8f6f4 v[172:175], v[152:159], v[184:191], v[84:87]
	v_mfma_f32_16x16x128_f8f6f4 v[176:179], v[160:167], v[184:191], v[76:79]
	v_mfma_f32_16x16x128_f8f6f4 v[180:183], v[152:159], v[192:199], v[68:71]
	v_mfma_f32_16x16x128_f8f6f4 v[184:187], v[160:167], v[192:199], v[64:67]
	s_setprio 0
	s_barrier
	s_mov_b32 m0, s57
	s_mov_b32 s10, s14
	s_mov_b32 s11, s15
	s_nop 1
	ds_read_b128 v[64:67], v252 offset:16384
	ds_read_b128 v[72:75], v252 offset:18432
	ds_read_b128 v[68:71], v253 offset:16384
	ds_read_b128 v[76:79], v253 offset:18432
	ds_read_b128 v[80:83], v252 offset:20480
	ds_read_b128 v[88:91], v252 offset:22528
	ds_read_b128 v[84:87], v253 offset:20480
	ds_read_b128 v[92:95], v253 offset:22528
	buffer_load_dwordx4 v244, s[8:11], s38 offen lds
	s_mov_b32 m0, s58
	s_add_i32 s41, s38, 0x40000
	buffer_load_dwordx4 v245, s[8:11], s38 offen lds
	s_mov_b32 m0, s59
	s_nop 0
	buffer_load_dwordx4 v244, s[8:11], s41 offen lds
	s_mov_b32 m0, s60
	s_nop 0
	buffer_load_dwordx4 v245, s[8:11], s41 offen lds
	s_waitcnt vmcnt(6)
	s_waitcnt lgkmcnt(0)
	s_barrier
	s_setprio 1
	s_mov_b32 m0, s56
	s_waitcnt lgkmcnt(5)
	v_mfma_f32_16x16x128_f8f6f4 v[60:63], v[136:143], v[64:71], v[60:63]
	v_mfma_f32_16x16x128_f8f6f4 v[56:59], v[144:151], v[64:71], v[56:59]
	s_waitcnt lgkmcnt(4)
	v_mfma_f32_16x16x128_f8f6f4 v[48:51], v[136:143], v[72:79], v[48:51]
	v_mfma_f32_16x16x128_f8f6f4 v[188:191], v[144:151], v[72:79], v[40:43]
	s_waitcnt lgkmcnt(1)
	v_mfma_f32_16x16x128_f8f6f4 v[192:195], v[136:143], v[80:87], v[32:35]
	buffer_load_dwordx4 v248, s[12:15], s40 offen lds
	s_mov_b32 m0, s61
	v_mfma_f32_16x16x128_f8f6f4 v[196:199], v[144:151], v[80:87], v[24:27]
	s_waitcnt lgkmcnt(0)
	v_mfma_f32_16x16x128_f8f6f4 v[208:211], v[136:143], v[88:95], v[16:19]
	v_mfma_f32_16x16x128_f8f6f4 v[212:215], v[144:151], v[88:95], v[8:11]
	v_mfma_f32_16x16x128_f8f6f4 v[52:55], v[152:159], v[64:71], v[52:55]
	v_mfma_f32_16x16x128_f8f6f4 v[216:219], v[160:167], v[64:71], v[44:47]
	v_mfma_f32_16x16x128_f8f6f4 v[220:223], v[152:159], v[72:79], v[36:39]
	buffer_load_dwordx4 v249, s[12:15], s40 offen lds
	v_mfma_f32_16x16x128_f8f6f4 v[224:227], v[160:167], v[72:79], v[28:31]
	v_mfma_f32_16x16x128_f8f6f4 v[228:231], v[152:159], v[80:87], v[20:23]
	v_mfma_f32_16x16x128_f8f6f4 v[232:235], v[160:167], v[80:87], v[12:15]
	v_mfma_f32_16x16x128_f8f6f4 v[236:239], v[152:159], v[88:95], v[4:7]
	v_mfma_f32_16x16x128_f8f6f4 v[240:243], v[160:167], v[88:95], v[0:3]
	s_setprio 0
	s_barrier
	s_add_i32 s41, 0, 0x18000
	s_nop 2
	v_add_u32_e32 v4, s41, v246
	v_add_u32_e32 v12, s41, v247
	s_add_i32 s41, 0, 0x1c000
	v_add_u32_e32 v16, s41, v246
	ds_read_b128 v[0:3], v4
	ds_read_b128 v[8:11], v4 offset:2048
	ds_read_b128 v[4:7], v12
	ds_read_b128 v[12:15], v12 offset:2048
	v_add_u32_e32 v17, s41, v247
	ds_read_b128 v[136:139], v16
	ds_read_b128 v[144:147], v16 offset:2048
	ds_read_b128 v[140:143], v17
	ds_read_b128 v[148:151], v17 offset:2048
	s_mov_b32 m0, s62
	ds_read_b128 v[16:19], v252 offset:32768
	ds_read_b128 v[24:27], v252 offset:34816
	ds_read_b128 v[20:23], v253 offset:32768
	ds_read_b128 v[28:31], v253 offset:34816
	ds_read_b128 v[32:35], v252 offset:36864
	ds_read_b128 v[40:43], v252 offset:38912
	ds_read_b128 v[36:39], v253 offset:36864
	ds_read_b128 v[44:47], v253 offset:38912
	buffer_load_dwordx4 v250, s[12:15], s40 offen lds
	s_mov_b32 m0, s63
	s_nop 0
	buffer_load_dwordx4 v251, s[12:15], s40 offen lds
	s_waitcnt vmcnt(8)
	s_waitcnt lgkmcnt(0)
	s_barrier
	s_setprio 1
	s_waitcnt lgkmcnt(5)
	v_mfma_f32_16x16x128_f8f6f4 v[124:127], v[0:7], v[16:23], v[124:127]
	v_mfma_f32_16x16x128_f8f6f4 v[120:123], v[8:15], v[16:23], v[120:123]
	s_waitcnt lgkmcnt(4)
	v_mfma_f32_16x16x128_f8f6f4 v[112:115], v[0:7], v[24:31], v[112:115]
	v_mfma_f32_16x16x128_f8f6f4 v[104:107], v[8:15], v[24:31], v[104:107]
	s_waitcnt lgkmcnt(1)
	v_mfma_f32_16x16x128_f8f6f4 v[96:99], v[0:7], v[32:39], v[96:99]
	v_mfma_f32_16x16x128_f8f6f4 v[88:91], v[8:15], v[32:39], v[128:131]
	s_waitcnt lgkmcnt(0)
	v_mfma_f32_16x16x128_f8f6f4 v[80:83], v[0:7], v[40:47], v[200:203]
	v_mfma_f32_16x16x128_f8f6f4 v[72:75], v[8:15], v[40:47], v[204:207]
	v_mfma_f32_16x16x128_f8f6f4 v[116:119], v[136:143], v[16:23], v[116:119]
	v_mfma_f32_16x16x128_f8f6f4 v[108:111], v[144:151], v[16:23], v[108:111]
	v_mfma_f32_16x16x128_f8f6f4 v[100:103], v[136:143], v[24:31], v[100:103]
	v_mfma_f32_16x16x128_f8f6f4 v[92:95], v[144:151], v[24:31], v[168:171]
	v_mfma_f32_16x16x128_f8f6f4 v[84:87], v[136:143], v[32:39], v[172:175]
	v_mfma_f32_16x16x128_f8f6f4 v[76:79], v[144:151], v[32:39], v[176:179]
	v_mfma_f32_16x16x128_f8f6f4 v[68:71], v[136:143], v[40:47], v[180:183]
	v_mfma_f32_16x16x128_f8f6f4 v[64:67], v[144:151], v[40:47], v[184:187]
	s_setprio 0
	s_barrier
	s_mov_b32 m0, s64
	s_add_i32 s40, s38, 0x80
	ds_read_b128 v[152:155], v252 offset:49152
	ds_read_b128 v[160:163], v252 offset:51200
	ds_read_b128 v[156:159], v253 offset:49152
	ds_read_b128 v[164:167], v253 offset:51200
	ds_read_b128 v[168:171], v252 offset:53248
	ds_read_b128 v[176:179], v252 offset:55296
	ds_read_b128 v[172:175], v253 offset:53248
	ds_read_b128 v[180:183], v253 offset:55296
	buffer_load_dwordx4 v244, s[8:11], s40 offen lds
	s_mov_b32 m0, s65
	s_add_i32 s38, s38, 0x40080
	buffer_load_dwordx4 v245, s[8:11], s40 offen lds
	s_mov_b32 m0, s68
	s_nop 0
	buffer_load_dwordx4 v244, s[8:11], s38 offen lds
	s_mov_b32 m0, s69
	s_nop 0
	buffer_load_dwordx4 v245, s[8:11], s38 offen lds
	s_waitcnt vmcnt(6)
	s_waitcnt lgkmcnt(0)
	s_barrier
	s_setprio 1
	s_mov_b32 m0, s66
	s_waitcnt lgkmcnt(5)
	v_mfma_f32_16x16x128_f8f6f4 v[60:63], v[0:7], v[152:159], v[60:63]
	v_mfma_f32_16x16x128_f8f6f4 v[56:59], v[8:15], v[152:159], v[56:59]
	s_waitcnt lgkmcnt(4)
	v_mfma_f32_16x16x128_f8f6f4 v[48:51], v[0:7], v[160:167], v[48:51]
	v_mfma_f32_16x16x128_f8f6f4 v[40:43], v[8:15], v[160:167], v[188:191]
	s_waitcnt lgkmcnt(1)
	v_mfma_f32_16x16x128_f8f6f4 v[32:35], v[0:7], v[168:175], v[192:195]
	buffer_load_dwordx4 v248, s[12:15], s39 offen lds
	s_mov_b32 m0, s67
	v_mfma_f32_16x16x128_f8f6f4 v[24:27], v[8:15], v[168:175], v[196:199]
	s_waitcnt lgkmcnt(0)
	v_mfma_f32_16x16x128_f8f6f4 v[16:19], v[0:7], v[176:183], v[208:211]
	v_mfma_f32_16x16x128_f8f6f4 v[8:11], v[8:15], v[176:183], v[212:215]
	v_mfma_f32_16x16x128_f8f6f4 v[52:55], v[136:143], v[152:159], v[52:55]
	v_mfma_f32_16x16x128_f8f6f4 v[44:47], v[144:151], v[152:159], v[216:219]
	v_mfma_f32_16x16x128_f8f6f4 v[36:39], v[136:143], v[160:167], v[220:223]
	buffer_load_dwordx4 v249, s[12:15], s39 offen lds
	v_mfma_f32_16x16x128_f8f6f4 v[28:31], v[144:151], v[160:167], v[224:227]
	v_mfma_f32_16x16x128_f8f6f4 v[20:23], v[136:143], v[168:175], v[228:231]
	v_mfma_f32_16x16x128_f8f6f4 v[12:15], v[144:151], v[168:175], v[232:235]
	v_mfma_f32_16x16x128_f8f6f4 v[4:7], v[136:143], v[176:183], v[236:239]
	v_mfma_f32_16x16x128_f8f6f4 v[0:3], v[144:151], v[176:183], v[240:243]
	s_setprio 0
	s_barrier
	s_add_i32 s96, s96, 2
	s_addk_i32 s97, 0x100
	s_cmp_gt_u32 s96, 13
	s_cbranch_scc1 .LBB0_1022

.Lp5_join:
	ds_read_b128 v[136:139], v129
	ds_read_b128 v[144:147], v129 offset:2048
	ds_read_b128 v[140:143], v130
	ds_read_b128 v[148:151], v130 offset:2048
	v_add_u32_e32 v129, s50, v244
	v_add_u32_e32 v130, s50, v245
	ds_read_b128 v[152:155], v129
	ds_read_b128 v[160:163], v129 offset:2048
	ds_read_b128 v[156:159], v130
	ds_read_b128 v[164:167], v130 offset:2048
	s_add_i32 s6, s62, 0xffffff80
	s_add_i32 s7, s6, s57
	s_cmpk_eq_i32 s62, 0x880
	s_cselect_b32 s65, s35, s54
	s_cselect_b32 s6, 0, s6
	s_cselect_b32 s64, 0x80, s62
	s_cselect_b32 s63, s29, s7
	s_add_i32 s7, s54, s62
	s_add_i32 s64, s65, s64
	s_addk_i32 s7, 0xff00
	s_add_i32 s65, s65, s6
	s_mov_b32 m0, s44
	ds_read_b128 v[168:171], v250
	ds_read_b128 v[176:179], v250 offset:2048
	ds_read_b128 v[172:175], v251
	ds_read_b128 v[180:183], v251 offset:2048
	ds_read_b128 v[184:187], v250 offset:4096
	ds_read_b128 v[192:195], v250 offset:6144
	ds_read_b128 v[188:191], v251 offset:4096
	ds_read_b128 v[196:199], v251 offset:6144
	buffer_load_dwordx4 v248, s[8:11], s7 offen lds
	s_mov_b32 m0, s47
	s_nop 0
	buffer_load_dwordx4 v249, s[8:11], s7 offen lds
	s_waitcnt vmcnt(8)
	s_waitcnt lgkmcnt(0)
	s_barrier
	s_setprio 1
	s_waitcnt lgkmcnt(5)
	v_mfma_f32_16x16x128_f8f6f4 v[124:127], v[136:143], v[168:175], v[124:127]
	v_mfma_f32_16x16x128_f8f6f4 v[120:123], v[144:151], v[168:175], v[120:123]
	s_waitcnt lgkmcnt(4)
	v_mfma_f32_16x16x128_f8f6f4 v[108:111], v[136:143], v[176:183], v[108:111]
	v_mfma_f32_16x16x128_f8f6f4 v[104:107], v[144:151], v[176:183], v[104:107]
	s_waitcnt lgkmcnt(1)
	v_mfma_f32_16x16x128_f8f6f4 v[128:131], v[136:143], v[184:191], v[92:95]
	v_mfma_f32_16x16x128_f8f6f4 v[200:203], v[144:151], v[184:191], v[88:91]
	s_waitcnt lgkmcnt(0)
	v_mfma_f32_16x16x128_f8f6f4 v[204:207], v[136:143], v[192:199], v[76:79]
	v_mfma_f32_16x16x128_f8f6f4 v[208:211], v[144:151], v[192:199], v[72:75]
	v_mfma_f32_16x16x128_f8f6f4 v[116:119], v[152:159], v[168:175], v[116:119]
	v_mfma_f32_16x16x128_f8f6f4 v[112:115], v[160:167], v[168:175], v[112:115]
	v_mfma_f32_16x16x128_f8f6f4 v[100:103], v[152:159], v[176:183], v[100:103]
	v_mfma_f32_16x16x128_f8f6f4 v[96:99], v[160:167], v[176:183], v[96:99]
	v_mfma_f32_16x16x128_f8f6f4 v[168:171], v[152:159], v[184:191], v[84:87]
	v_mfma_f32_16x16x128_f8f6f4 v[172:175], v[160:167], v[184:191], v[80:83]
	v_mfma_f32_16x16x128_f8f6f4 v[176:179], v[152:159], v[192:199], v[68:71]
	v_mfma_f32_16x16x128_f8f6f4 v[180:183], v[160:167], v[192:199], v[64:67]
	s_setprio 0
	s_barrier
	s_mov_b32 m0, s26
	s_mov_b32 s6, s10
	s_mov_b32 s7, s11
	s_nop 1
	ds_read_b128 v[64:67], v250 offset:16384
	ds_read_b128 v[72:75], v250 offset:18432
	ds_read_b128 v[68:71], v251 offset:16384
	ds_read_b128 v[76:79], v251 offset:18432
	ds_read_b128 v[80:83], v250 offset:20480
	ds_read_b128 v[88:91], v250 offset:22528
	ds_read_b128 v[84:87], v251 offset:20480
	ds_read_b128 v[92:95], v251 offset:22528
	buffer_load_dwordx4 v132, s[4:7], s63 offen lds
	s_mov_b32 m0, s27
	s_add_i32 s66, s63, 0x40000
	buffer_load_dwordx4 v133, s[4:7], s63 offen lds
	s_mov_b32 m0, s28
	s_nop 0
	buffer_load_dwordx4 v132, s[4:7], s66 offen lds
	s_mov_b32 m0, s30
	s_nop 0
	buffer_load_dwordx4 v133, s[4:7], s66 offen lds
	s_waitcnt vmcnt(6)
	s_waitcnt lgkmcnt(0)
	s_barrier
	s_setprio 1
	s_mov_b32 m0, s25
	s_waitcnt lgkmcnt(5)
	v_mfma_f32_16x16x128_f8f6f4 v[60:63], v[136:143], v[64:71], v[60:63]
	v_mfma_f32_16x16x128_f8f6f4 v[56:59], v[144:151], v[64:71], v[56:59]
	s_waitcnt lgkmcnt(4)
	v_mfma_f32_16x16x128_f8f6f4 v[184:187], v[136:143], v[72:79], v[44:47]
	v_mfma_f32_16x16x128_f8f6f4 v[188:191], v[144:151], v[72:79], v[40:43]
	s_waitcnt lgkmcnt(1)
	v_mfma_f32_16x16x128_f8f6f4 v[192:195], v[136:143], v[80:87], v[28:31]
	buffer_load_dwordx4 v246, s[8:11], s65 offen lds
	s_mov_b32 m0, s31
	v_mfma_f32_16x16x128_f8f6f4 v[196:199], v[144:151], v[80:87], v[24:27]
	s_waitcnt lgkmcnt(0)
	v_mfma_f32_16x16x128_f8f6f4 v[212:215], v[136:143], v[88:95], v[12:15]
	v_mfma_f32_16x16x128_f8f6f4 v[216:219], v[144:151], v[88:95], v[8:11]
	v_mfma_f32_16x16x128_f8f6f4 v[52:55], v[152:159], v[64:71], v[52:55]
	v_mfma_f32_16x16x128_f8f6f4 v[48:51], v[160:167], v[64:71], v[48:51]
	v_mfma_f32_16x16x128_f8f6f4 v[220:223], v[152:159], v[72:79], v[36:39]
	buffer_load_dwordx4 v247, s[8:11], s65 offen lds
	v_mfma_f32_16x16x128_f8f6f4 v[224:227], v[160:167], v[72:79], v[32:35]
	v_mfma_f32_16x16x128_f8f6f4 v[228:231], v[152:159], v[80:87], v[20:23]
	v_mfma_f32_16x16x128_f8f6f4 v[232:235], v[160:167], v[80:87], v[16:19]
	v_mfma_f32_16x16x128_f8f6f4 v[236:239], v[152:159], v[88:95], v[4:7]
	v_mfma_f32_16x16x128_f8f6f4 v[240:243], v[160:167], v[88:95], v[0:3]
	s_setprio 0
	s_barrier
	s_add_i32 s66, 0, 0x18000
	s_nop 2
	v_add_u32_e32 v4, s66, v244
	v_add_u32_e32 v8, s66, v245
	s_add_i32 s66, 0, 0x1c000
	ds_read_b128 v[0:3], v4
	ds_read_b128 v[16:19], v4 offset:2048
	ds_read_b128 v[4:7], v8
	ds_read_b128 v[20:23], v8 offset:2048
	v_add_u32_e32 v8, s66, v244
	v_add_u32_e32 v9, s66, v245
	ds_read_b128 v[136:139], v8
	ds_read_b128 v[144:147], v8 offset:2048
	ds_read_b128 v[140:143], v9
	ds_read_b128 v[148:151], v9 offset:2048
	s_mov_b32 m0, s33
	ds_read_b128 v[8:11], v250 offset:32768
	ds_read_b128 v[24:27], v250 offset:34816
	ds_read_b128 v[12:15], v251 offset:32768
	ds_read_b128 v[28:31], v251 offset:34816
	ds_read_b128 v[32:35], v250 offset:36864
	ds_read_b128 v[40:43], v250 offset:38912
	ds_read_b128 v[36:39], v251 offset:36864
	ds_read_b128 v[44:47], v251 offset:38912
	buffer_load_dwordx4 v248, s[8:11], s65 offen lds
	s_mov_b32 m0, s34
	s_nop 0
	buffer_load_dwordx4 v249, s[8:11], s65 offen lds
	s_waitcnt vmcnt(8)
	s_waitcnt lgkmcnt(0)
	s_barrier
	s_setprio 1
	s_waitcnt lgkmcnt(5)
	v_mfma_f32_16x16x128_f8f6f4 v[124:127], v[0:7], v[8:15], v[124:127]
	v_mfma_f32_16x16x128_f8f6f4 v[120:123], v[16:23], v[8:15], v[120:123]
	s_waitcnt lgkmcnt(4)
	v_mfma_f32_16x16x128_f8f6f4 v[108:111], v[0:7], v[24:31], v[108:111]
	v_mfma_f32_16x16x128_f8f6f4 v[104:107], v[16:23], v[24:31], v[104:107]
	s_waitcnt lgkmcnt(1)
	v_mfma_f32_16x16x128_f8f6f4 v[92:95], v[0:7], v[32:39], v[128:131]
	v_mfma_f32_16x16x128_f8f6f4 v[88:91], v[16:23], v[32:39], v[200:203]
	s_waitcnt lgkmcnt(0)
	v_mfma_f32_16x16x128_f8f6f4 v[76:79], v[0:7], v[40:47], v[204:207]
	v_mfma_f32_16x16x128_f8f6f4 v[72:75], v[16:23], v[40:47], v[208:211]
	v_mfma_f32_16x16x128_f8f6f4 v[116:119], v[136:143], v[8:15], v[116:119]
	v_mfma_f32_16x16x128_f8f6f4 v[112:115], v[144:151], v[8:15], v[112:115]
	v_mfma_f32_16x16x128_f8f6f4 v[100:103], v[136:143], v[24:31], v[100:103]
	v_mfma_f32_16x16x128_f8f6f4 v[96:99], v[144:151], v[24:31], v[96:99]
	v_mfma_f32_16x16x128_f8f6f4 v[84:87], v[136:143], v[32:39], v[168:171]
	v_mfma_f32_16x16x128_f8f6f4 v[80:83], v[144:151], v[32:39], v[172:175]
	v_mfma_f32_16x16x128_f8f6f4 v[68:71], v[136:143], v[40:47], v[176:179]
	v_mfma_f32_16x16x128_f8f6f4 v[64:67], v[144:151], v[40:47], v[180:183]
	s_setprio 0
	s_barrier
	s_mov_b32 m0, s36
	s_add_i32 s65, s63, 0x80
	ds_read_b128 v[32:35], v250 offset:49152
	ds_read_b128 v[152:155], v250 offset:51200
	ds_read_b128 v[36:39], v251 offset:49152
	ds_read_b128 v[156:159], v251 offset:51200
	ds_read_b128 v[160:163], v250 offset:53248
	ds_read_b128 v[168:171], v250 offset:55296
	ds_read_b128 v[164:167], v251 offset:53248
	ds_read_b128 v[172:175], v251 offset:55296
	buffer_load_dwordx4 v132, s[4:7], s65 offen lds
	s_mov_b32 m0, s37
	s_add_i32 s63, s63, 0x40080
	buffer_load_dwordx4 v133, s[4:7], s65 offen lds
	s_mov_b32 m0, s40
	s_nop 0
	buffer_load_dwordx4 v132, s[4:7], s63 offen lds
	s_mov_b32 m0, s41
	s_nop 0
	buffer_load_dwordx4 v133, s[4:7], s63 offen lds
	s_waitcnt vmcnt(6)
	s_waitcnt lgkmcnt(0)
	s_barrier
	s_setprio 1
	s_mov_b32 m0, s38
	s_waitcnt lgkmcnt(5)
	v_mfma_f32_16x16x128_f8f6f4 v[60:63], v[0:7], v[32:39], v[60:63]
	v_mfma_f32_16x16x128_f8f6f4 v[56:59], v[16:23], v[32:39], v[56:59]
	s_waitcnt lgkmcnt(4)
	v_mfma_f32_16x16x128_f8f6f4 v[44:47], v[0:7], v[152:159], v[184:187]
	v_mfma_f32_16x16x128_f8f6f4 v[40:43], v[16:23], v[152:159], v[188:191]
	s_waitcnt lgkmcnt(1)
	v_mfma_f32_16x16x128_f8f6f4 v[28:31], v[0:7], v[160:167], v[192:195]
	buffer_load_dwordx4 v246, s[8:11], s64 offen lds
	s_mov_b32 m0, s39
	v_mfma_f32_16x16x128_f8f6f4 v[24:27], v[16:23], v[160:167], v[196:199]
	s_waitcnt lgkmcnt(0)
	v_mfma_f32_16x16x128_f8f6f4 v[12:15], v[0:7], v[168:175], v[212:215]
	v_mfma_f32_16x16x128_f8f6f4 v[8:11], v[16:23], v[168:175], v[216:219]
	v_mfma_f32_16x16x128_f8f6f4 v[52:55], v[136:143], v[32:39], v[52:55]
	v_mfma_f32_16x16x128_f8f6f4 v[48:51], v[144:151], v[32:39], v[48:51]
	v_mfma_f32_16x16x128_f8f6f4 v[36:39], v[136:143], v[152:159], v[220:223]
	buffer_load_dwordx4 v247, s[8:11], s64 offen lds
	v_mfma_f32_16x16x128_f8f6f4 v[32:35], v[144:151], v[152:159], v[224:227]
	v_mfma_f32_16x16x128_f8f6f4 v[20:23], v[136:143], v[160:167], v[228:231]
	v_mfma_f32_16x16x128_f8f6f4 v[16:19], v[144:151], v[160:167], v[232:235]
	v_mfma_f32_16x16x128_f8f6f4 v[4:7], v[136:143], v[168:175], v[236:239]
	v_mfma_f32_16x16x128_f8f6f4 v[0:3], v[144:151], v[168:175], v[240:243]
	s_setprio 0
	s_barrier
	s_add_i32 s61, s61, 2
	s_addk_i32 s62, 0x100
	s_cmp_gt_u32 s61, 13
	s_cbranch_scc1 .LBB0_2177

.Lp6_join:
	ds_read_b128 v[128:131], v132
	ds_read_b128 v[136:139], v132 offset:2048
	ds_read_b128 v[132:135], v140
	ds_read_b128 v[140:143], v140 offset:2048
	v_add_u32_e32 v155, s52, v246
	ds_read_b128 v[144:147], v148
	ds_read_b128 v[160:163], v148 offset:2048
	ds_read_b128 v[148:151], v155
	ds_read_b128 v[164:167], v155 offset:2048
	s_add_i32 s6, s64, 0xffffff80
	s_add_i32 s7, s6, s59
	s_cmpk_eq_i32 s64, 0x880
	s_cselect_b32 s67, s37, s56
	s_cselect_b32 s6, 0, s6
	s_cselect_b32 s66, 0x80, s64
	s_cselect_b32 s65, s31, s7
	s_add_i32 s7, s56, s64
	s_add_i32 s66, s67, s66
	s_addk_i32 s7, 0xff00
	s_add_i32 s67, s67, s6
	s_mov_b32 m0, s46
	ds_read_b128 v[168:171], v251
	ds_read_b128 v[176:179], v251 offset:2048
	ds_read_b128 v[172:175], v252
	ds_read_b128 v[180:183], v252 offset:2048
	ds_read_b128 v[184:187], v251 offset:4096
	ds_read_b128 v[192:195], v251 offset:6144
	ds_read_b128 v[188:191], v252 offset:4096
	ds_read_b128 v[196:199], v252 offset:6144
	buffer_load_dwordx4 v249, s[8:11], s7 offen lds
	s_mov_b32 m0, s49
	s_nop 0
	buffer_load_dwordx4 v250, s[8:11], s7 offen lds
	s_waitcnt vmcnt(8)
	s_waitcnt lgkmcnt(0)
	s_barrier
	s_setprio 1
	s_waitcnt lgkmcnt(5)
	v_mfma_f32_16x16x128_f8f6f4 v[124:127], v[128:135], v[168:175], v[124:127]
	v_mfma_f32_16x16x128_f8f6f4 v[120:123], v[136:143], v[168:175], v[120:123]
	s_waitcnt lgkmcnt(4)
	v_mfma_f32_16x16x128_f8f6f4 v[108:111], v[128:135], v[176:183], v[108:111]
	v_mfma_f32_16x16x128_f8f6f4 v[104:107], v[136:143], v[176:183], v[104:107]
	s_waitcnt lgkmcnt(1)
	v_mfma_f32_16x16x128_f8f6f4 v[152:155], v[128:135], v[184:191], v[92:95]
	v_mfma_f32_16x16x128_f8f6f4 v[200:203], v[136:143], v[184:191], v[88:91]
	s_waitcnt lgkmcnt(0)
	v_mfma_f32_16x16x128_f8f6f4 v[204:207], v[128:135], v[192:199], v[76:79]
	v_mfma_f32_16x16x128_f8f6f4 v[208:211], v[136:143], v[192:199], v[72:75]
	v_mfma_f32_16x16x128_f8f6f4 v[116:119], v[144:151], v[168:175], v[116:119]
	v_mfma_f32_16x16x128_f8f6f4 v[112:115], v[160:167], v[168:175], v[112:115]
	v_mfma_f32_16x16x128_f8f6f4 v[100:103], v[144:151], v[176:183], v[100:103]
	v_mfma_f32_16x16x128_f8f6f4 v[96:99], v[160:167], v[176:183], v[96:99]
	v_mfma_f32_16x16x128_f8f6f4 v[168:171], v[144:151], v[184:191], v[84:87]
	v_mfma_f32_16x16x128_f8f6f4 v[172:175], v[160:167], v[184:191], v[80:83]
	v_mfma_f32_16x16x128_f8f6f4 v[176:179], v[144:151], v[192:199], v[68:71]
	v_mfma_f32_16x16x128_f8f6f4 v[180:183], v[160:167], v[192:199], v[64:67]
	s_setprio 0
	s_barrier
	s_mov_b32 m0, s28
	s_mov_b32 s6, s10
	s_mov_b32 s7, s11
	s_nop 1
	ds_read_b128 v[64:67], v251 offset:16384
	ds_read_b128 v[72:75], v251 offset:18432
	ds_read_b128 v[68:71], v252 offset:16384
	ds_read_b128 v[76:79], v252 offset:18432
	ds_read_b128 v[80:83], v251 offset:20480
	ds_read_b128 v[88:91], v251 offset:22528
	ds_read_b128 v[84:87], v252 offset:20480
	ds_read_b128 v[92:95], v252 offset:22528
	buffer_load_dwordx4 v159, s[4:7], s65 offen lds
	s_mov_b32 m0, s29
	s_add_i32 s68, s65, 0x40000
	buffer_load_dwordx4 v244, s[4:7], s65 offen lds
	s_mov_b32 m0, s30
	s_nop 0
	buffer_load_dwordx4 v159, s[4:7], s68 offen lds
	s_mov_b32 m0, s33
	s_nop 0
	buffer_load_dwordx4 v244, s[4:7], s68 offen lds
	s_waitcnt vmcnt(6)
	s_waitcnt lgkmcnt(0)
	s_barrier
	s_setprio 1
	s_mov_b32 m0, s27
	s_waitcnt lgkmcnt(5)
	v_mfma_f32_16x16x128_f8f6f4 v[60:63], v[128:135], v[64:71], v[60:63]
	v_mfma_f32_16x16x128_f8f6f4 v[56:59], v[136:143], v[64:71], v[56:59]
	s_waitcnt lgkmcnt(4)
	v_mfma_f32_16x16x128_f8f6f4 v[184:187], v[128:135], v[72:79], v[44:47]
	v_mfma_f32_16x16x128_f8f6f4 v[188:191], v[136:143], v[72:79], v[40:43]
	s_waitcnt lgkmcnt(1)
	v_mfma_f32_16x16x128_f8f6f4 v[192:195], v[128:135], v[80:87], v[28:31]
	buffer_load_dwordx4 v247, s[8:11], s67 offen lds
	s_mov_b32 m0, s34
	v_mfma_f32_16x16x128_f8f6f4 v[196:199], v[136:143], v[80:87], v[24:27]
	s_waitcnt lgkmcnt(0)
	v_mfma_f32_16x16x128_f8f6f4 v[212:215], v[128:135], v[88:95], v[12:15]
	v_mfma_f32_16x16x128_f8f6f4 v[216:219], v[136:143], v[88:95], v[8:11]
	v_mfma_f32_16x16x128_f8f6f4 v[52:55], v[144:151], v[64:71], v[52:55]
	v_mfma_f32_16x16x128_f8f6f4 v[48:51], v[160:167], v[64:71], v[48:51]
	v_mfma_f32_16x16x128_f8f6f4 v[220:223], v[144:151], v[72:79], v[36:39]
	buffer_load_dwordx4 v248, s[8:11], s67 offen lds
	v_mfma_f32_16x16x128_f8f6f4 v[224:227], v[160:167], v[72:79], v[32:35]
	v_mfma_f32_16x16x128_f8f6f4 v[228:231], v[144:151], v[80:87], v[20:23]
	v_mfma_f32_16x16x128_f8f6f4 v[232:235], v[160:167], v[80:87], v[16:19]
	v_mfma_f32_16x16x128_f8f6f4 v[236:239], v[144:151], v[88:95], v[4:7]
	v_mfma_f32_16x16x128_f8f6f4 v[240:243], v[160:167], v[88:95], v[0:3]
	s_setprio 0
	s_barrier
	s_add_i32 s68, 0, 0x18000
	s_nop 2
	v_add_u32_e32 v4, s68, v245
	v_add_u32_e32 v8, s68, v246
	s_add_i32 s68, 0, 0x1c000
	ds_read_b128 v[0:3], v4
	ds_read_b128 v[16:19], v4 offset:2048
	ds_read_b128 v[4:7], v8
	ds_read_b128 v[20:23], v8 offset:2048
	v_add_u32_e32 v8, s68, v245
	v_add_u32_e32 v9, s68, v246
	ds_read_b128 v[128:131], v8
	ds_read_b128 v[136:139], v8 offset:2048
	ds_read_b128 v[132:135], v9
	ds_read_b128 v[140:143], v9 offset:2048
	s_mov_b32 m0, s35
	ds_read_b128 v[8:11], v251 offset:32768
	ds_read_b128 v[24:27], v251 offset:34816
	ds_read_b128 v[12:15], v252 offset:32768
	ds_read_b128 v[28:31], v252 offset:34816
	ds_read_b128 v[32:35], v251 offset:36864
	ds_read_b128 v[40:43], v251 offset:38912
	ds_read_b128 v[36:39], v252 offset:36864
	ds_read_b128 v[44:47], v252 offset:38912
	buffer_load_dwordx4 v249, s[8:11], s67 offen lds
	s_mov_b32 m0, s36
	s_nop 0
	buffer_load_dwordx4 v250, s[8:11], s67 offen lds
	s_waitcnt vmcnt(8)
	s_waitcnt lgkmcnt(0)
	s_barrier
	s_setprio 1
	s_waitcnt lgkmcnt(5)
	v_mfma_f32_16x16x128_f8f6f4 v[124:127], v[0:7], v[8:15], v[124:127]
	v_mfma_f32_16x16x128_f8f6f4 v[120:123], v[16:23], v[8:15], v[120:123]
	s_waitcnt lgkmcnt(4)
	v_mfma_f32_16x16x128_f8f6f4 v[108:111], v[0:7], v[24:31], v[108:111]
	v_mfma_f32_16x16x128_f8f6f4 v[104:107], v[16:23], v[24:31], v[104:107]
	s_waitcnt lgkmcnt(1)
	v_mfma_f32_16x16x128_f8f6f4 v[92:95], v[0:7], v[32:39], v[152:155]
	v_mfma_f32_16x16x128_f8f6f4 v[88:91], v[16:23], v[32:39], v[200:203]
	s_waitcnt lgkmcnt(0)
	v_mfma_f32_16x16x128_f8f6f4 v[76:79], v[0:7], v[40:47], v[204:207]
	v_mfma_f32_16x16x128_f8f6f4 v[72:75], v[16:23], v[40:47], v[208:211]
	v_mfma_f32_16x16x128_f8f6f4 v[116:119], v[128:135], v[8:15], v[116:119]
	v_mfma_f32_16x16x128_f8f6f4 v[112:115], v[136:143], v[8:15], v[112:115]
	v_mfma_f32_16x16x128_f8f6f4 v[100:103], v[128:135], v[24:31], v[100:103]
	v_mfma_f32_16x16x128_f8f6f4 v[96:99], v[136:143], v[24:31], v[96:99]
	v_mfma_f32_16x16x128_f8f6f4 v[84:87], v[128:135], v[32:39], v[168:171]
	v_mfma_f32_16x16x128_f8f6f4 v[80:83], v[136:143], v[32:39], v[172:175]
	v_mfma_f32_16x16x128_f8f6f4 v[68:71], v[128:135], v[40:47], v[176:179]
	v_mfma_f32_16x16x128_f8f6f4 v[64:67], v[136:143], v[40:47], v[180:183]
	s_setprio 0
	s_barrier
	s_mov_b32 m0, s38
	s_add_i32 s67, s65, 0x80
	ds_read_b128 v[32:35], v251 offset:49152
	ds_read_b128 v[144:147], v251 offset:51200
	ds_read_b128 v[36:39], v252 offset:49152
	ds_read_b128 v[148:151], v252 offset:51200
	ds_read_b128 v[160:163], v251 offset:53248
	ds_read_b128 v[168:171], v251 offset:55296
	ds_read_b128 v[164:167], v252 offset:53248
	ds_read_b128 v[172:175], v252 offset:55296
	buffer_load_dwordx4 v159, s[4:7], s67 offen lds
	s_mov_b32 m0, s39
	s_add_i32 s65, s65, 0x40080
	buffer_load_dwordx4 v244, s[4:7], s67 offen lds
	s_mov_b32 m0, s42
	s_nop 0
	buffer_load_dwordx4 v159, s[4:7], s65 offen lds
	s_mov_b32 m0, s43
	s_nop 0
	buffer_load_dwordx4 v244, s[4:7], s65 offen lds
	s_waitcnt vmcnt(6)
	s_waitcnt lgkmcnt(0)
	s_barrier
	s_setprio 1
	s_mov_b32 m0, s40
	s_waitcnt lgkmcnt(5)
	v_mfma_f32_16x16x128_f8f6f4 v[60:63], v[0:7], v[32:39], v[60:63]
	v_mfma_f32_16x16x128_f8f6f4 v[56:59], v[16:23], v[32:39], v[56:59]
	s_waitcnt lgkmcnt(4)
	v_mfma_f32_16x16x128_f8f6f4 v[44:47], v[0:7], v[144:151], v[184:187]
	v_mfma_f32_16x16x128_f8f6f4 v[40:43], v[16:23], v[144:151], v[188:191]
	s_waitcnt lgkmcnt(1)
	v_mfma_f32_16x16x128_f8f6f4 v[28:31], v[0:7], v[160:167], v[192:195]
	buffer_load_dwordx4 v247, s[8:11], s66 offen lds
	s_mov_b32 m0, s41
	v_mfma_f32_16x16x128_f8f6f4 v[24:27], v[16:23], v[160:167], v[196:199]
	s_waitcnt lgkmcnt(0)
	v_mfma_f32_16x16x128_f8f6f4 v[12:15], v[0:7], v[168:175], v[212:215]
	v_mfma_f32_16x16x128_f8f6f4 v[8:11], v[16:23], v[168:175], v[216:219]
	v_mfma_f32_16x16x128_f8f6f4 v[52:55], v[128:135], v[32:39], v[52:55]
	v_mfma_f32_16x16x128_f8f6f4 v[48:51], v[136:143], v[32:39], v[48:51]
	v_mfma_f32_16x16x128_f8f6f4 v[36:39], v[128:135], v[144:151], v[220:223]
	buffer_load_dwordx4 v248, s[8:11], s66 offen lds
	v_mfma_f32_16x16x128_f8f6f4 v[32:35], v[136:143], v[144:151], v[224:227]
	v_mfma_f32_16x16x128_f8f6f4 v[20:23], v[128:135], v[160:167], v[228:231]
	v_mfma_f32_16x16x128_f8f6f4 v[16:19], v[136:143], v[160:167], v[232:235]
	v_mfma_f32_16x16x128_f8f6f4 v[4:7], v[128:135], v[168:175], v[236:239]
	v_mfma_f32_16x16x128_f8f6f4 v[0:3], v[136:143], v[168:175], v[240:243]
	s_setprio 0
	s_barrier
	s_add_i32 s63, s63, 2
	s_addk_i32 s64, 0x100
	s_cmp_gt_u32 s63, 13
	s_cbranch_scc1 .LBB0_2201

.Lp7_join:
	ds_read_b128 v[128:131], v132
	ds_read_b128 v[138:141], v132 offset:2048
	ds_read_b128 v[132:135], v142
	ds_read_b128 v[142:145], v142 offset:2048
	ds_read_b128 v[146:149], v150
	ds_read_b128 v[154:157], v150 offset:2048
	ds_read_b128 v[150:153], v158
	ds_read_b128 v[158:161], v158 offset:2048
	s_add_i32 s6, s61, 0xffffff80
	s_add_i32 s7, s6, s56
	s_cmpk_eq_i32 s61, 0x880
	s_cselect_b32 s64, s35, s53
	s_cselect_b32 s6, 0, s6
	s_cselect_b32 s63, 0x80, s61
	s_cselect_b32 s62, s29, s7
	s_add_i32 s7, s53, s61
	s_add_i32 s63, s64, s63
	s_addk_i32 s7, 0xff00
	s_add_i32 s64, s64, s6
	s_mov_b32 m0, s44
	ds_read_b128 v[162:165], v250
	ds_read_b128 v[170:173], v250 offset:2048
	ds_read_b128 v[166:169], v251
	ds_read_b128 v[174:177], v251 offset:2048
	ds_read_b128 v[178:181], v250 offset:4096
	ds_read_b128 v[186:189], v250 offset:6144
	ds_read_b128 v[182:185], v251 offset:4096
	ds_read_b128 v[190:193], v251 offset:6144
	buffer_load_dwordx4 v248, s[8:11], s7 offen lds
	s_mov_b32 m0, s47
	s_nop 0
	buffer_load_dwordx4 v249, s[8:11], s7 offen lds
	s_waitcnt vmcnt(8)
	s_waitcnt lgkmcnt(0)
	s_barrier
	s_setprio 1
	s_waitcnt lgkmcnt(0)
	v_mfma_f32_16x16x128_f8f6f4 v[124:127], v[128:135], v[162:169], v[124:127]
	v_mfma_f32_16x16x128_f8f6f4 v[120:123], v[138:145], v[162:169], v[120:123]
	v_mfma_f32_16x16x128_f8f6f4 v[116:119], v[128:135], v[170:177], v[116:119]
	v_mfma_f32_16x16x128_f8f6f4 v[112:115], v[138:145], v[170:177], v[112:115]
	v_mfma_f32_16x16x128_f8f6f4 v[194:197], v[128:135], v[178:185], v[92:95]
	v_mfma_f32_16x16x128_f8f6f4 v[198:201], v[138:145], v[178:185], v[88:91]
	v_mfma_f32_16x16x128_f8f6f4 v[202:205], v[128:135], v[186:193], v[84:87]
	v_mfma_f32_16x16x128_f8f6f4 v[206:209], v[138:145], v[186:193], v[80:83]
	v_mfma_f32_16x16x128_f8f6f4 v[108:111], v[146:153], v[162:169], v[108:111]
	v_mfma_f32_16x16x128_f8f6f4 v[104:107], v[154:161], v[162:169], v[104:107]
	v_mfma_f32_16x16x128_f8f6f4 v[100:103], v[146:153], v[170:177], v[100:103]
	v_mfma_f32_16x16x128_f8f6f4 v[96:99], v[154:161], v[170:177], v[96:99]
	v_mfma_f32_16x16x128_f8f6f4 v[162:165], v[146:153], v[178:185], v[76:79]
	v_mfma_f32_16x16x128_f8f6f4 v[166:169], v[154:161], v[178:185], v[72:75]
	v_mfma_f32_16x16x128_f8f6f4 v[170:173], v[146:153], v[186:193], v[68:71]
	v_mfma_f32_16x16x128_f8f6f4 v[174:177], v[154:161], v[186:193], v[64:67]
	s_setprio 0
	s_barrier
	s_mov_b32 m0, s26
	s_mov_b32 s6, s10
	s_mov_b32 s7, s11
	s_nop 1
	ds_read_b128 v[64:67], v250 offset:16384
	ds_read_b128 v[72:75], v250 offset:18432
	ds_read_b128 v[68:71], v251 offset:16384
	ds_read_b128 v[76:79], v251 offset:18432
	ds_read_b128 v[80:83], v250 offset:20480
	ds_read_b128 v[88:91], v250 offset:22528
	ds_read_b128 v[84:87], v251 offset:20480
	ds_read_b128 v[92:95], v251 offset:22528
	buffer_load_dwordx4 v242, s[4:7], s62 offen lds
	s_mov_b32 m0, s27
	s_add_i32 s65, s62, 0x40000
	buffer_load_dwordx4 v243, s[4:7], s62 offen lds
	s_mov_b32 m0, s28
	s_nop 0
	buffer_load_dwordx4 v242, s[4:7], s65 offen lds
	s_mov_b32 m0, s30
	s_nop 0
	buffer_load_dwordx4 v243, s[4:7], s65 offen lds
	s_waitcnt vmcnt(6)
	s_waitcnt lgkmcnt(0)
	s_barrier
	s_setprio 1
	s_mov_b32 m0, s25
	s_waitcnt lgkmcnt(5)
	v_mfma_f32_16x16x128_f8f6f4 v[60:63], v[128:135], v[64:71], v[60:63]
	v_mfma_f32_16x16x128_f8f6f4 v[56:59], v[138:145], v[64:71], v[56:59]
	s_waitcnt lgkmcnt(4)
	v_mfma_f32_16x16x128_f8f6f4 v[52:55], v[128:135], v[72:79], v[52:55]
	v_mfma_f32_16x16x128_f8f6f4 v[48:51], v[138:145], v[72:79], v[48:51]
	s_waitcnt lgkmcnt(1)
	v_mfma_f32_16x16x128_f8f6f4 v[178:181], v[128:135], v[80:87], v[28:31]
	buffer_load_dwordx4 v246, s[8:11], s64 offen lds
	s_mov_b32 m0, s31
	v_mfma_f32_16x16x128_f8f6f4 v[182:185], v[138:145], v[80:87], v[24:27]
	s_waitcnt lgkmcnt(0)
	v_mfma_f32_16x16x128_f8f6f4 v[186:189], v[128:135], v[88:95], v[20:23]
	v_mfma_f32_16x16x128_f8f6f4 v[190:193], v[138:145], v[88:95], v[16:19]
	v_mfma_f32_16x16x128_f8f6f4 v[210:213], v[146:153], v[64:71], v[44:47]
	v_mfma_f32_16x16x128_f8f6f4 v[214:217], v[154:161], v[64:71], v[40:43]
	v_mfma_f32_16x16x128_f8f6f4 v[218:221], v[146:153], v[72:79], v[36:39]
	buffer_load_dwordx4 v247, s[8:11], s64 offen lds
	v_mfma_f32_16x16x128_f8f6f4 v[222:225], v[154:161], v[72:79], v[32:35]
	v_mfma_f32_16x16x128_f8f6f4 v[226:229], v[146:153], v[80:87], v[12:15]
	v_mfma_f32_16x16x128_f8f6f4 v[230:233], v[154:161], v[80:87], v[8:11]
	v_mfma_f32_16x16x128_f8f6f4 v[234:237], v[146:153], v[88:95], v[4:7]
	v_mfma_f32_16x16x128_f8f6f4 v[238:241], v[154:161], v[88:95], v[0:3]
	s_setprio 0
	s_barrier
	s_add_i32 s65, 0, 0x18000
	s_nop 2
	v_add_u32_e32 v4, s65, v244
	v_add_u32_e32 v12, s65, v245
	s_add_i32 s65, 0, 0x1c000
	v_add_u32_e32 v16, s65, v244
	ds_read_b128 v[0:3], v4
	ds_read_b128 v[8:11], v4 offset:2048
	ds_read_b128 v[4:7], v12
	ds_read_b128 v[12:15], v12 offset:2048
	v_add_u32_e32 v17, s65, v245
	ds_read_b128 v[128:131], v16
	ds_read_b128 v[138:141], v16 offset:2048
	ds_read_b128 v[132:135], v17
	ds_read_b128 v[142:145], v17 offset:2048
	s_mov_b32 m0, s33
	ds_read_b128 v[16:19], v250 offset:32768
	ds_read_b128 v[24:27], v250 offset:34816
	ds_read_b128 v[20:23], v251 offset:32768
	ds_read_b128 v[28:31], v251 offset:34816
	ds_read_b128 v[32:35], v250 offset:36864
	ds_read_b128 v[40:43], v250 offset:38912
	ds_read_b128 v[36:39], v251 offset:36864
	ds_read_b128 v[44:47], v251 offset:38912
	buffer_load_dwordx4 v248, s[8:11], s64 offen lds
	s_mov_b32 m0, s34
	s_nop 0
	buffer_load_dwordx4 v249, s[8:11], s64 offen lds
	s_waitcnt vmcnt(8)
	s_waitcnt lgkmcnt(0)
	s_barrier
	s_setprio 1
	s_waitcnt lgkmcnt(5)
	v_mfma_f32_16x16x128_f8f6f4 v[124:127], v[0:7], v[16:23], v[124:127]
	v_mfma_f32_16x16x128_f8f6f4 v[120:123], v[8:15], v[16:23], v[120:123]
	s_waitcnt lgkmcnt(4)
	v_mfma_f32_16x16x128_f8f6f4 v[116:119], v[0:7], v[24:31], v[116:119]
	v_mfma_f32_16x16x128_f8f6f4 v[112:115], v[8:15], v[24:31], v[112:115]
	s_waitcnt lgkmcnt(1)
	v_mfma_f32_16x16x128_f8f6f4 v[92:95], v[0:7], v[32:39], v[194:197]
	v_mfma_f32_16x16x128_f8f6f4 v[88:91], v[8:15], v[32:39], v[198:201]
	s_waitcnt lgkmcnt(0)
	v_mfma_f32_16x16x128_f8f6f4 v[84:87], v[0:7], v[40:47], v[202:205]
	v_mfma_f32_16x16x128_f8f6f4 v[80:83], v[8:15], v[40:47], v[206:209]
	v_mfma_f32_16x16x128_f8f6f4 v[108:111], v[128:135], v[16:23], v[108:111]
	v_mfma_f32_16x16x128_f8f6f4 v[104:107], v[138:145], v[16:23], v[104:107]
	v_mfma_f32_16x16x128_f8f6f4 v[100:103], v[128:135], v[24:31], v[100:103]
	v_mfma_f32_16x16x128_f8f6f4 v[96:99], v[138:145], v[24:31], v[96:99]
	v_mfma_f32_16x16x128_f8f6f4 v[76:79], v[128:135], v[32:39], v[162:165]
	v_mfma_f32_16x16x128_f8f6f4 v[72:75], v[138:145], v[32:39], v[166:169]
	v_mfma_f32_16x16x128_f8f6f4 v[68:71], v[128:135], v[40:47], v[170:173]
	v_mfma_f32_16x16x128_f8f6f4 v[64:67], v[138:145], v[40:47], v[174:177]
	s_setprio 0
	s_barrier
	s_mov_b32 m0, s36
	s_add_i32 s64, s62, 0x80
	ds_read_b128 v[32:35], v250 offset:49152
	ds_read_b128 v[146:149], v250 offset:51200
	ds_read_b128 v[36:39], v251 offset:49152
	ds_read_b128 v[150:153], v251 offset:51200
	ds_read_b128 v[154:157], v250 offset:53248
	ds_read_b128 v[162:165], v250 offset:55296
	ds_read_b128 v[158:161], v251 offset:53248
	ds_read_b128 v[166:169], v251 offset:55296
	buffer_load_dwordx4 v242, s[4:7], s64 offen lds
	s_mov_b32 m0, s37
	s_add_i32 s62, s62, 0x40080
	buffer_load_dwordx4 v243, s[4:7], s64 offen lds
	s_mov_b32 m0, s40
	s_nop 0
	buffer_load_dwordx4 v242, s[4:7], s62 offen lds
	s_mov_b32 m0, s41
	s_nop 0
	buffer_load_dwordx4 v243, s[4:7], s62 offen lds
	s_waitcnt vmcnt(6)
	s_waitcnt lgkmcnt(0)
	s_barrier
	s_setprio 1
	s_mov_b32 m0, s38
	s_waitcnt lgkmcnt(5)
	v_mfma_f32_16x16x128_f8f6f4 v[60:63], v[0:7], v[32:39], v[60:63]
	v_mfma_f32_16x16x128_f8f6f4 v[56:59], v[8:15], v[32:39], v[56:59]
	s_waitcnt lgkmcnt(4)
	v_mfma_f32_16x16x128_f8f6f4 v[52:55], v[0:7], v[146:153], v[52:55]
	v_mfma_f32_16x16x128_f8f6f4 v[48:51], v[8:15], v[146:153], v[48:51]
	s_waitcnt lgkmcnt(1)
	v_mfma_f32_16x16x128_f8f6f4 v[28:31], v[0:7], v[154:161], v[178:181]
	buffer_load_dwordx4 v246, s[8:11], s63 offen lds
	s_mov_b32 m0, s39
	v_mfma_f32_16x16x128_f8f6f4 v[24:27], v[8:15], v[154:161], v[182:185]
	s_waitcnt lgkmcnt(0)
	v_mfma_f32_16x16x128_f8f6f4 v[20:23], v[0:7], v[162:169], v[186:189]
	v_mfma_f32_16x16x128_f8f6f4 v[16:19], v[8:15], v[162:169], v[190:193]
	v_mfma_f32_16x16x128_f8f6f4 v[44:47], v[128:135], v[32:39], v[210:213]
	v_mfma_f32_16x16x128_f8f6f4 v[40:43], v[138:145], v[32:39], v[214:217]
	v_mfma_f32_16x16x128_f8f6f4 v[36:39], v[128:135], v[146:153], v[218:221]
	buffer_load_dwordx4 v247, s[8:11], s63 offen lds
	v_mfma_f32_16x16x128_f8f6f4 v[32:35], v[138:145], v[146:153], v[222:225]
	v_mfma_f32_16x16x128_f8f6f4 v[12:15], v[128:135], v[154:161], v[226:229]
	v_mfma_f32_16x16x128_f8f6f4 v[8:11], v[138:145], v[154:161], v[230:233]
	v_mfma_f32_16x16x128_f8f6f4 v[4:7], v[128:135], v[162:169], v[234:237]
	v_mfma_f32_16x16x128_f8f6f4 v[0:3], v[138:145], v[162:169], v[238:241]
	s_setprio 0
	s_barrier
	s_add_i32 s60, s60, 2
	s_addk_i32 s61, 0x100
	s_cmp_gt_u32 s60, 13
	s_cbranch_scc1 .LBB0_2279

.LBB0_2473:
	v_lshlrev_b32_e32 v206, 1, v203
	v_lshrrev_b32_e32 v207, 2, v203
	s_add_i32 s10, s82, 0xffffff80
	v_and_b32_e32 v206, 24, v206
	v_and_b32_e32 v207, 4, v207
	v_and_b32_e32 v203, 0x1fffe3, v203
	s_waitcnt vmcnt(8)
	s_add_i32 s14, s77, 2
	s_add_i32 s11, s10, s76
	v_or3_b32 v203, v203, v207, v206
	v_lshlrev_b32_e32 v206, 1, v202
	v_lshrrev_b32_e32 v207, 2, v202
	s_waitcnt lgkmcnt(0)
	s_and_b64 s[6:7], s[6:7], exec
	v_and_b32_e32 v206, 24, v206
	v_and_b32_e32 v207, 4, v207
	v_and_b32_e32 v202, 0x1fffe3, v202
	s_cselect_b32 s7, s46, s11
	v_or3_b32 v202, v202, v207, v206
	s_cselect_b32 s6, 0x80, s82
	s_cselect_b32 s83, 0, s10
	s_add_i32 s15, s7, 0x80
	v_lshl_or_b32 v203, v203, 11, v201
	v_lshl_or_b32 v201, v202, 11, v201
	s_barrier
	s_setprio 1
	s_waitcnt lgkmcnt(0)
	v_mfma_f32_16x16x128_f8f6f4 v[192:195], v[16:23], v[40:47], v[192:195]
	v_mfma_f32_16x16x128_f8f6f4 v[188:191], v[24:31], v[40:47], v[188:191]
	v_mfma_f32_16x16x128_f8f6f4 v[176:179], v[16:23], v[32:39], v[176:179]
	v_mfma_f32_16x16x128_f8f6f4 v[168:171], v[24:31], v[32:39], v[168:171]
	v_mfma_f32_16x16x128_f8f6f4 v[160:163], v[16:23], v[56:63], v[160:163]
	v_mfma_f32_16x16x128_f8f6f4 v[152:155], v[24:31], v[56:63], v[152:155]
	v_mfma_f32_16x16x128_f8f6f4 v[144:147], v[16:23], v[48:55], v[144:147]
	v_mfma_f32_16x16x128_f8f6f4 v[136:139], v[24:31], v[48:55], v[136:139]
	v_mfma_f32_16x16x128_f8f6f4 v[184:187], v[0:7], v[40:47], v[184:187]
	v_mfma_f32_16x16x128_f8f6f4 v[180:183], v[8:15], v[40:47], v[180:183]
	v_mfma_f32_16x16x128_f8f6f4 v[172:175], v[0:7], v[32:39], v[172:175]
	v_mfma_f32_16x16x128_f8f6f4 v[164:167], v[8:15], v[32:39], v[164:167]
	v_mfma_f32_16x16x128_f8f6f4 v[156:159], v[0:7], v[56:63], v[156:159]
	v_mfma_f32_16x16x128_f8f6f4 v[148:151], v[8:15], v[56:63], v[148:151]
	v_mfma_f32_16x16x128_f8f6f4 v[140:143], v[0:7], v[48:55], v[140:143]
	v_mfma_f32_16x16x128_f8f6f4 v[132:135], v[8:15], v[48:55], v[132:135]
	s_setprio 0
	s_barrier
	s_mov_b32 m0, s50
	s_mov_b32 s10, s18
	s_mov_b32 s11, s19
	ds_read_b128 v[32:35], v200 offset:16384
	ds_read_b128 v[40:43], v200 offset:18432
	ds_read_b128 v[36:39], v199 offset:16384
	ds_read_b128 v[44:47], v199 offset:18432
	ds_read_b128 v[48:51], v200 offset:20480
	ds_read_b128 v[56:59], v200 offset:22528
	ds_read_b128 v[52:55], v199 offset:20480
	ds_read_b128 v[60:63], v199 offset:22528
	buffer_load_dwordx4 v203, s[8:11], s7 offen lds
	s_mov_b32 m0, s51
	s_add_i32 s84, s7, 0x40000
	buffer_load_dwordx4 v201, s[8:11], s7 offen lds
	s_mov_b32 m0, s52
	s_nop 0
	buffer_load_dwordx4 v203, s[8:11], s84 offen lds
	s_mov_b32 m0, s53
	s_nop 0
	buffer_load_dwordx4 v201, s[8:11], s84 offen lds
	s_waitcnt vmcnt(6)
	s_waitcnt lgkmcnt(0)
	s_barrier
	s_setprio 1
	s_mov_b32 m0, s49
	s_waitcnt lgkmcnt(5)
	v_mfma_f32_16x16x128_f8f6f4 v[128:131], v[16:23], v[32:39], v[128:131]
	v_mfma_f32_16x16x128_f8f6f4 v[120:123], v[24:31], v[32:39], v[120:123]
	s_waitcnt lgkmcnt(4)
	v_mfma_f32_16x16x128_f8f6f4 v[112:115], v[16:23], v[40:47], v[112:115]
	v_mfma_f32_16x16x128_f8f6f4 v[104:107], v[24:31], v[40:47], v[104:107]
	s_waitcnt lgkmcnt(1)
	v_mfma_f32_16x16x128_f8f6f4 v[96:99], v[16:23], v[48:55], v[96:99]
	buffer_load_dwordx4 v64, s[16:19], s83 offen lds
	s_mov_b32 m0, s54
	v_mfma_f32_16x16x128_f8f6f4 v[88:91], v[24:31], v[48:55], v[88:91]
	s_waitcnt lgkmcnt(0)
	v_mfma_f32_16x16x128_f8f6f4 v[80:83], v[16:23], v[56:63], v[80:83]
	v_mfma_f32_16x16x128_f8f6f4 v[72:75], v[24:31], v[56:63], v[72:75]
	v_mfma_f32_16x16x128_f8f6f4 v[124:127], v[0:7], v[32:39], v[124:127]
	v_mfma_f32_16x16x128_f8f6f4 v[116:119], v[8:15], v[32:39], v[116:119]
	v_mfma_f32_16x16x128_f8f6f4 v[108:111], v[0:7], v[40:47], v[108:111]
	buffer_load_dwordx4 v65, s[16:19], s83 offen lds
	v_mfma_f32_16x16x128_f8f6f4 v[100:103], v[8:15], v[40:47], v[100:103]
	v_mfma_f32_16x16x128_f8f6f4 v[92:95], v[0:7], v[48:55], v[92:95]
	v_mfma_f32_16x16x128_f8f6f4 v[84:87], v[8:15], v[48:55], v[84:87]
	v_mfma_f32_16x16x128_f8f6f4 v[76:79], v[0:7], v[56:63], v[76:79]
	v_mfma_f32_16x16x128_f8f6f4 v[68:71], v[8:15], v[56:63], v[68:71]
	s_setprio 0
	s_barrier
	s_add_i32 s84, 0, 0x18000
	v_add_u32_e32 v4, s84, v204
	v_add_u32_e32 v12, s84, v205
	s_add_i32 s84, 0, 0x1c000
	v_add_u32_e32 v20, s84, v204
	v_add_u32_e32 v28, s84, v205
	ds_read_b128 v[0:3], v4
	ds_read_b128 v[8:11], v4 offset:2048
	ds_read_b128 v[4:7], v12
	ds_read_b128 v[12:15], v12 offset:2048
	ds_read_b128 v[16:19], v20
	ds_read_b128 v[24:27], v20 offset:2048
	ds_read_b128 v[20:23], v28
	ds_read_b128 v[28:31], v28 offset:2048
	s_mov_b32 m0, s55
	ds_read_b128 v[32:35], v200 offset:32768
	ds_read_b128 v[40:43], v200 offset:34816
	ds_read_b128 v[36:39], v199 offset:32768
	ds_read_b128 v[44:47], v199 offset:34816
	ds_read_b128 v[48:51], v200 offset:36864
	ds_read_b128 v[56:59], v200 offset:38912
	ds_read_b128 v[52:55], v199 offset:36864
	ds_read_b128 v[60:63], v199 offset:38912
	buffer_load_dwordx4 v66, s[16:19], s83 offen lds
	s_mov_b32 m0, s56
	s_nop 0
	buffer_load_dwordx4 v67, s[16:19], s83 offen lds
	s_waitcnt vmcnt(8)
	s_waitcnt lgkmcnt(0)
	s_barrier
	s_setprio 1
	s_waitcnt lgkmcnt(5)
	v_mfma_f32_16x16x128_f8f6f4 v[192:195], v[0:7], v[32:39], v[192:195]
	v_mfma_f32_16x16x128_f8f6f4 v[188:191], v[8:15], v[32:39], v[188:191]
	s_waitcnt lgkmcnt(4)
	v_mfma_f32_16x16x128_f8f6f4 v[176:179], v[0:7], v[40:47], v[176:179]
	v_mfma_f32_16x16x128_f8f6f4 v[168:171], v[8:15], v[40:47], v[168:171]
	s_waitcnt lgkmcnt(1)
	v_mfma_f32_16x16x128_f8f6f4 v[160:163], v[0:7], v[48:55], v[160:163]
	v_mfma_f32_16x16x128_f8f6f4 v[152:155], v[8:15], v[48:55], v[152:155]
	s_waitcnt lgkmcnt(0)
	v_mfma_f32_16x16x128_f8f6f4 v[144:147], v[0:7], v[56:63], v[144:147]
	v_mfma_f32_16x16x128_f8f6f4 v[136:139], v[8:15], v[56:63], v[136:139]
	v_mfma_f32_16x16x128_f8f6f4 v[184:187], v[16:23], v[32:39], v[184:187]
	v_mfma_f32_16x16x128_f8f6f4 v[180:183], v[24:31], v[32:39], v[180:183]
	v_mfma_f32_16x16x128_f8f6f4 v[172:175], v[16:23], v[40:47], v[172:175]
	v_mfma_f32_16x16x128_f8f6f4 v[164:167], v[24:31], v[40:47], v[164:167]
	v_mfma_f32_16x16x128_f8f6f4 v[156:159], v[16:23], v[48:55], v[156:159]
	v_mfma_f32_16x16x128_f8f6f4 v[148:151], v[24:31], v[48:55], v[148:151]
	v_mfma_f32_16x16x128_f8f6f4 v[140:143], v[16:23], v[56:63], v[140:143]
	v_mfma_f32_16x16x128_f8f6f4 v[132:135], v[24:31], v[56:63], v[132:135]
	s_setprio 0
	s_barrier
	s_mov_b32 m0, s58
	ds_read_b128 v[32:35], v200 offset:49152
	ds_read_b128 v[40:43], v200 offset:51200
	ds_read_b128 v[36:39], v199 offset:49152
	ds_read_b128 v[44:47], v199 offset:51200
	ds_read_b128 v[48:51], v200 offset:53248
	ds_read_b128 v[56:59], v200 offset:55296
	ds_read_b128 v[52:55], v199 offset:53248
	ds_read_b128 v[60:63], v199 offset:55296
	buffer_load_dwordx4 v203, s[8:11], s15 offen lds
	s_mov_b32 m0, s59
	s_add_i32 s7, s7, 0x40080
	buffer_load_dwordx4 v201, s[8:11], s15 offen lds
	s_mov_b32 m0, s62
	s_nop 0
	buffer_load_dwordx4 v203, s[8:11], s7 offen lds
	s_mov_b32 m0, s63
	s_nop 0
	buffer_load_dwordx4 v201, s[8:11], s7 offen lds
	s_waitcnt vmcnt(6)
	s_waitcnt lgkmcnt(0)
	s_barrier
	s_setprio 1
	s_mov_b32 m0, s60
	s_waitcnt lgkmcnt(5)
	v_mfma_f32_16x16x128_f8f6f4 v[128:131], v[0:7], v[32:39], v[128:131]
	v_mfma_f32_16x16x128_f8f6f4 v[120:123], v[8:15], v[32:39], v[120:123]
	s_waitcnt lgkmcnt(4)
	v_mfma_f32_16x16x128_f8f6f4 v[112:115], v[0:7], v[40:47], v[112:115]
	v_mfma_f32_16x16x128_f8f6f4 v[104:107], v[8:15], v[40:47], v[104:107]
	s_waitcnt lgkmcnt(1)
	v_mfma_f32_16x16x128_f8f6f4 v[96:99], v[0:7], v[48:55], v[96:99]
	buffer_load_dwordx4 v64, s[16:19], s6 offen lds
	s_mov_b32 m0, s61
	v_mfma_f32_16x16x128_f8f6f4 v[88:91], v[8:15], v[48:55], v[88:91]
	s_waitcnt lgkmcnt(0)
	v_mfma_f32_16x16x128_f8f6f4 v[80:83], v[0:7], v[56:63], v[80:83]
	v_mfma_f32_16x16x128_f8f6f4 v[72:75], v[8:15], v[56:63], v[72:75]
	v_mfma_f32_16x16x128_f8f6f4 v[124:127], v[16:23], v[32:39], v[124:127]
	v_mfma_f32_16x16x128_f8f6f4 v[116:119], v[24:31], v[32:39], v[116:119]
	v_mfma_f32_16x16x128_f8f6f4 v[108:111], v[16:23], v[40:47], v[108:111]
	buffer_load_dwordx4 v65, s[16:19], s6 offen lds
	v_mfma_f32_16x16x128_f8f6f4 v[100:103], v[24:31], v[40:47], v[100:103]
	v_mfma_f32_16x16x128_f8f6f4 v[92:95], v[16:23], v[48:55], v[92:95]
	v_mfma_f32_16x16x128_f8f6f4 v[84:87], v[24:31], v[48:55], v[84:87]
	v_mfma_f32_16x16x128_f8f6f4 v[76:79], v[16:23], v[56:63], v[76:79]
	v_mfma_f32_16x16x128_f8f6f4 v[68:71], v[24:31], v[56:63], v[68:71]
	s_setprio 0
	s_barrier
	s_addk_i32 s82, 0x100
	s_cmp_gt_u32 s77, 13
	s_cbranch_scc1 .LBB0_2479
	s_mov_b32 s77, s14
	s_branch .LBB0_2454

.Lp11_join:
	ds_read_b128 v[128:131], v132
	ds_read_b128 v[136:139], v132 offset:2048
	ds_read_b128 v[132:135], v140
	ds_read_b128 v[140:143], v140 offset:2048
	ds_read_b128 v[154:157], v158
	ds_read_b128 v[162:165], v158 offset:2048
	ds_read_b128 v[158:161], v166
	ds_read_b128 v[166:169], v166 offset:2048
	s_add_i32 s6, s80, 0xffffff80
	s_add_i32 s7, s6, s75
	s_cmpk_eq_i32 s80, 0x880
	s_cselect_b32 s81, s71, s35
	s_cselect_b32 s11, 0x80, s80
	s_cselect_b32 s10, 0, s6
	s_cselect_b32 s6, s51, s7
	s_add_i32 s7, s81, s11
	s_add_i32 s11, s35, s80
	s_addk_i32 s11, 0xff00
	s_add_i32 s81, s81, s10
	s_mov_b32 m0, s60
	ds_read_b128 v[170:173], v148
	ds_read_b128 v[178:181], v148 offset:2048
	ds_read_b128 v[174:177], v146
	ds_read_b128 v[182:185], v146 offset:2048
	ds_read_b128 v[186:189], v148 offset:4096
	ds_read_b128 v[194:197], v148 offset:6144
	ds_read_b128 v[190:193], v146 offset:4096
	ds_read_b128 v[198:201], v146 offset:6144
	buffer_load_dwordx4 v252, s[88:91], s11 offen lds
	s_mov_b32 m0, s63
	s_nop 0
	buffer_load_dwordx4 v253, s[88:91], s11 offen lds
	s_waitcnt vmcnt(8)
	s_waitcnt lgkmcnt(0)
	s_barrier
	s_setprio 1
	s_waitcnt lgkmcnt(0)
	v_mfma_f32_16x16x128_f8f6f4 v[124:127], v[128:135], v[170:177], v[124:127]
	v_mfma_f32_16x16x128_f8f6f4 v[120:123], v[136:143], v[170:177], v[120:123]
	v_mfma_f32_16x16x128_f8f6f4 v[116:119], v[128:135], v[178:185], v[116:119]
	v_mfma_f32_16x16x128_f8f6f4 v[112:115], v[136:143], v[178:185], v[112:115]
	v_mfma_f32_16x16x128_f8f6f4 v[96:99], v[128:135], v[186:193], v[96:99]
	v_mfma_f32_16x16x128_f8f6f4 v[202:205], v[136:143], v[186:193], v[88:91]
	v_mfma_f32_16x16x128_f8f6f4 v[206:209], v[128:135], v[194:201], v[80:83]
	v_mfma_f32_16x16x128_f8f6f4 v[210:213], v[136:143], v[194:201], v[72:75]
	v_mfma_f32_16x16x128_f8f6f4 v[108:111], v[154:161], v[170:177], v[108:111]
	v_mfma_f32_16x16x128_f8f6f4 v[104:107], v[162:169], v[170:177], v[104:107]
	v_mfma_f32_16x16x128_f8f6f4 v[100:103], v[154:161], v[178:185], v[100:103]
	v_mfma_f32_16x16x128_f8f6f4 v[170:173], v[162:169], v[178:185], v[92:95]
	v_mfma_f32_16x16x128_f8f6f4 v[174:177], v[154:161], v[186:193], v[84:87]
	v_mfma_f32_16x16x128_f8f6f4 v[178:181], v[162:169], v[186:193], v[76:79]
	v_mfma_f32_16x16x128_f8f6f4 v[182:185], v[154:161], v[194:201], v[68:71]
	v_mfma_f32_16x16x128_f8f6f4 v[186:189], v[162:169], v[194:201], v[64:67]
	s_setprio 0
	s_barrier
	s_mov_b32 m0, s43
	s_mov_b32 s10, s90
	s_mov_b32 s11, s91
	s_nop 1
	ds_read_b128 v[64:67], v148 offset:16384
	ds_read_b128 v[72:75], v148 offset:18432
	ds_read_b128 v[68:71], v146 offset:16384
	ds_read_b128 v[76:79], v146 offset:18432
	ds_read_b128 v[80:83], v148 offset:20480
	ds_read_b128 v[88:91], v148 offset:22528
	ds_read_b128 v[84:87], v146 offset:20480
	ds_read_b128 v[92:95], v146 offset:22528
	buffer_load_dwordx4 v144, s[8:11], s6 offen lds
	s_mov_b32 m0, s44
	s_add_i32 s82, s6, 0x40000
	buffer_load_dwordx4 v145, s[8:11], s6 offen lds
	s_mov_b32 m0, s45
	s_nop 0
	buffer_load_dwordx4 v144, s[8:11], s82 offen lds
	s_mov_b32 m0, s46
	s_nop 0
	buffer_load_dwordx4 v145, s[8:11], s82 offen lds
	s_waitcnt vmcnt(6)
	s_waitcnt lgkmcnt(0)
	s_barrier
	s_setprio 1
	s_mov_b32 m0, s42
	s_waitcnt lgkmcnt(5)
	v_mfma_f32_16x16x128_f8f6f4 v[60:63], v[128:135], v[64:71], v[60:63]
	v_mfma_f32_16x16x128_f8f6f4 v[56:59], v[136:143], v[64:71], v[56:59]
	s_waitcnt lgkmcnt(4)
	v_mfma_f32_16x16x128_f8f6f4 v[48:51], v[128:135], v[72:79], v[48:51]
	v_mfma_f32_16x16x128_f8f6f4 v[190:193], v[136:143], v[72:79], v[40:43]
	s_waitcnt lgkmcnt(1)
	v_mfma_f32_16x16x128_f8f6f4 v[194:197], v[128:135], v[80:87], v[32:35]
	buffer_load_dwordx4 v250, s[88:91], s81 offen lds
	s_mov_b32 m0, s47
	v_mfma_f32_16x16x128_f8f6f4 v[198:201], v[136:143], v[80:87], v[24:27]
	s_waitcnt lgkmcnt(0)
	v_mfma_f32_16x16x128_f8f6f4 v[214:217], v[128:135], v[88:95], v[16:19]
	v_mfma_f32_16x16x128_f8f6f4 v[218:221], v[136:143], v[88:95], v[8:11]
	v_mfma_f32_16x16x128_f8f6f4 v[52:55], v[154:161], v[64:71], v[52:55]
	v_mfma_f32_16x16x128_f8f6f4 v[222:225], v[162:169], v[64:71], v[44:47]
	v_mfma_f32_16x16x128_f8f6f4 v[226:229], v[154:161], v[72:79], v[36:39]
	buffer_load_dwordx4 v251, s[88:91], s81 offen lds
	v_mfma_f32_16x16x128_f8f6f4 v[230:233], v[162:169], v[72:79], v[28:31]
	v_mfma_f32_16x16x128_f8f6f4 v[234:237], v[154:161], v[80:87], v[20:23]
	v_mfma_f32_16x16x128_f8f6f4 v[238:241], v[162:169], v[80:87], v[12:15]
	v_mfma_f32_16x16x128_f8f6f4 v[242:245], v[154:161], v[88:95], v[4:7]
	v_mfma_f32_16x16x128_f8f6f4 v[246:249], v[162:169], v[88:95], v[0:3]
	s_setprio 0
	s_barrier
	s_add_i32 s82, 0, 0x18000
	s_nop 2
	v_add_u32_e32 v4, s82, v150
	v_add_u32_e32 v12, s82, v152
	s_add_i32 s82, 0, 0x1c000
	v_add_u32_e32 v16, s82, v150
	ds_read_b128 v[0:3], v4
	ds_read_b128 v[8:11], v4 offset:2048
	ds_read_b128 v[4:7], v12
	ds_read_b128 v[12:15], v12 offset:2048
	v_add_u32_e32 v17, s82, v152
	ds_read_b128 v[128:131], v16
	ds_read_b128 v[136:139], v16 offset:2048
	ds_read_b128 v[132:135], v17
	ds_read_b128 v[140:143], v17 offset:2048
	s_mov_b32 m0, s48
	ds_read_b128 v[16:19], v148 offset:32768
	ds_read_b128 v[24:27], v148 offset:34816
	ds_read_b128 v[20:23], v146 offset:32768
	ds_read_b128 v[28:31], v146 offset:34816
	ds_read_b128 v[32:35], v148 offset:36864
	ds_read_b128 v[40:43], v148 offset:38912
	ds_read_b128 v[36:39], v146 offset:36864
	ds_read_b128 v[44:47], v146 offset:38912
	buffer_load_dwordx4 v252, s[88:91], s81 offen lds
	s_mov_b32 m0, s49
	s_nop 0
	buffer_load_dwordx4 v253, s[88:91], s81 offen lds
	s_waitcnt vmcnt(8)
	s_waitcnt lgkmcnt(0)
	s_barrier
	s_setprio 1
	s_waitcnt lgkmcnt(5)
	v_mfma_f32_16x16x128_f8f6f4 v[124:127], v[0:7], v[16:23], v[124:127]
	v_mfma_f32_16x16x128_f8f6f4 v[120:123], v[8:15], v[16:23], v[120:123]
	s_waitcnt lgkmcnt(4)
	v_mfma_f32_16x16x128_f8f6f4 v[116:119], v[0:7], v[24:31], v[116:119]
	v_mfma_f32_16x16x128_f8f6f4 v[112:115], v[8:15], v[24:31], v[112:115]
	s_waitcnt lgkmcnt(1)
	v_mfma_f32_16x16x128_f8f6f4 v[96:99], v[0:7], v[32:39], v[96:99]
	v_mfma_f32_16x16x128_f8f6f4 v[88:91], v[8:15], v[32:39], v[202:205]
	s_waitcnt lgkmcnt(0)
	v_mfma_f32_16x16x128_f8f6f4 v[80:83], v[0:7], v[40:47], v[206:209]
	v_mfma_f32_16x16x128_f8f6f4 v[72:75], v[8:15], v[40:47], v[210:213]
	v_mfma_f32_16x16x128_f8f6f4 v[108:111], v[128:135], v[16:23], v[108:111]
	v_mfma_f32_16x16x128_f8f6f4 v[104:107], v[136:143], v[16:23], v[104:107]
	v_mfma_f32_16x16x128_f8f6f4 v[100:103], v[128:135], v[24:31], v[100:103]
	v_mfma_f32_16x16x128_f8f6f4 v[92:95], v[136:143], v[24:31], v[170:173]
	v_mfma_f32_16x16x128_f8f6f4 v[84:87], v[128:135], v[32:39], v[174:177]
	v_mfma_f32_16x16x128_f8f6f4 v[76:79], v[136:143], v[32:39], v[178:181]
	v_mfma_f32_16x16x128_f8f6f4 v[68:71], v[128:135], v[40:47], v[182:185]
	v_mfma_f32_16x16x128_f8f6f4 v[64:67], v[136:143], v[40:47], v[186:189]
	s_setprio 0
	s_barrier
	s_mov_b32 m0, s52
	s_add_i32 s81, s6, 0x80
	ds_read_b128 v[154:157], v148 offset:49152
	ds_read_b128 v[162:165], v148 offset:51200
	ds_read_b128 v[158:161], v146 offset:49152
	ds_read_b128 v[166:169], v146 offset:51200
	ds_read_b128 v[170:173], v148 offset:53248
	ds_read_b128 v[178:181], v148 offset:55296
	ds_read_b128 v[174:177], v146 offset:53248
	ds_read_b128 v[182:185], v146 offset:55296
	buffer_load_dwordx4 v144, s[8:11], s81 offen lds
	s_mov_b32 m0, s53
	s_add_i32 s6, s6, 0x40080
	buffer_load_dwordx4 v145, s[8:11], s81 offen lds
	s_mov_b32 m0, s56
	s_nop 0
	buffer_load_dwordx4 v144, s[8:11], s6 offen lds
	s_mov_b32 m0, s57
	s_nop 0
	buffer_load_dwordx4 v145, s[8:11], s6 offen lds
	s_waitcnt vmcnt(6)
	s_waitcnt lgkmcnt(0)
	s_barrier
	s_setprio 1
	s_mov_b32 m0, s54
	s_waitcnt lgkmcnt(5)
	v_mfma_f32_16x16x128_f8f6f4 v[60:63], v[0:7], v[154:161], v[60:63]
	v_mfma_f32_16x16x128_f8f6f4 v[56:59], v[8:15], v[154:161], v[56:59]
	s_waitcnt lgkmcnt(4)
	v_mfma_f32_16x16x128_f8f6f4 v[48:51], v[0:7], v[162:169], v[48:51]
	v_mfma_f32_16x16x128_f8f6f4 v[40:43], v[8:15], v[162:169], v[190:193]
	s_waitcnt lgkmcnt(1)
	v_mfma_f32_16x16x128_f8f6f4 v[32:35], v[0:7], v[170:177], v[194:197]
	buffer_load_dwordx4 v250, s[88:91], s7 offen lds
	s_mov_b32 m0, s55
	v_mfma_f32_16x16x128_f8f6f4 v[24:27], v[8:15], v[170:177], v[198:201]
	s_waitcnt lgkmcnt(0)
	v_mfma_f32_16x16x128_f8f6f4 v[16:19], v[0:7], v[178:185], v[214:217]
	v_mfma_f32_16x16x128_f8f6f4 v[8:11], v[8:15], v[178:185], v[218:221]
	v_mfma_f32_16x16x128_f8f6f4 v[52:55], v[128:135], v[154:161], v[52:55]
	v_mfma_f32_16x16x128_f8f6f4 v[44:47], v[136:143], v[154:161], v[222:225]
	v_mfma_f32_16x16x128_f8f6f4 v[36:39], v[128:135], v[162:169], v[226:229]
	buffer_load_dwordx4 v251, s[88:91], s7 offen lds
	v_mfma_f32_16x16x128_f8f6f4 v[28:31], v[136:143], v[162:169], v[230:233]
	v_mfma_f32_16x16x128_f8f6f4 v[20:23], v[128:135], v[170:177], v[234:237]
	v_mfma_f32_16x16x128_f8f6f4 v[12:15], v[136:143], v[170:177], v[238:241]
	v_mfma_f32_16x16x128_f8f6f4 v[4:7], v[128:135], v[178:185], v[242:245]
	v_mfma_f32_16x16x128_f8f6f4 v[0:3], v[136:143], v[178:185], v[246:249]
	s_setprio 0
	s_barrier
	s_add_i32 s79, s79, 2
	s_addk_i32 s80, 0x100
	s_cmp_gt_u32 s79, 13
	s_cbranch_scc1 .LBB0_2574
